# S5 GEMM a epilogue rewritten: one dispatch on the column tile, YI stored as 16-byte pieces (n=0/1 fragments exchanged across the four lane rows with permlane32/16 swaps) instead of 32 exec-masked 8-by
# speedup vs baseline: 1.0175x; 1.0019x over previous
; __device__ __forceinline__ unsigned cvt_pk_bf16(float lo, float hi) { const f32x2c v = {lo, hi}; const bf16x2c b = __builtin_convertvector(v, bf16x2c); return __builtin_bit_cast(unsigned, b); }
;     __device__ __forceinline__ void operator()(const f32x4 (&acc)[2][2][4][2], const Unit& u, int wr, int wc, int fr, int fq) const {
;         const int row0 = u.pm * BM + wr * 64 + fr, col0 = u.pn * BM + wc * 32 + 4 * fq;
; #pragma unroll
;         for (int ai = 0; ai < 2; ++ai)
; #pragma unroll
;             for (int m = 0; m < 4; ++m) { const size_t row = (size_t)(row0 + ai * HALF + m * 16);
; #pragma unroll
;                 for (int bj = 0; bj < 2; ++bj)
; #pragma unroll
;                     for (int n = 0; n < 2; ++n) { const int col = col0 + bj * HALF + 16 * n; const f32x4 v = acc[ai][bj][m][n];
;                         if (col < 512) { uint2 w; w.x = cvt_pk_bf16(v[0], v[1]); w.y = cvt_pk_bf16(v[2], v[3]); *(uint2*)(YI + row * 512 + col) = w; }
;                         else if (col < 640) *(f32x4*)(F + row * 128 + (col - 512)) = v; } }
.LBB0_266:
	v_lshl_add_u32 v140, s34, 8, v146
	s_lshl_b32 s21, s4, 8
	v_ashrrev_i32_e32 v141, 31, v140
	v_mov_b32_e32 v139, v133
	s_cmpk_lt_u32 s21, 0x200
	s_cbranch_scc0 .Ls5a_f
	v_and_b32_e32 v138, 12, v148
	v_add_u32_e32 v138, v138, v148
	v_or_b32_e32 v138, s21, v138
	v_lshlrev_b32_e32 v138, 1, v138
	v_lshlrev_b64 v[142:143], 10, v[140:141]
	v_lshl_add_u64 v[142:143], s[30:31], 0, v[142:143]
	v_lshl_add_u64 v[142:143], v[142:143], 0, v[138:139]
	v_cvt_pk_bf16_f32 v123, v122, v123
	v_cvt_pk_bf16_f32 v122, v120, v121
	v_cvt_pk_bf16_f32 v120, v124, v125
	v_cvt_pk_bf16_f32 v121, v126, v127
	v_cvt_pk_bf16_f32 v115, v114, v115
	v_cvt_pk_bf16_f32 v114, v112, v113
	v_cvt_pk_bf16_f32 v112, v116, v117
	v_cvt_pk_bf16_f32 v113, v118, v119
	v_permlane32_swap_b32_e32 v120, v122
	v_permlane32_swap_b32_e32 v121, v123
	v_permlane32_swap_b32_e32 v112, v114
	v_permlane32_swap_b32_e32 v113, v115
	v_permlane16_swap_b32_e32 v120, v122
	v_permlane16_swap_b32_e32 v121, v123
	v_permlane16_swap_b32_e32 v112, v114
	v_permlane16_swap_b32_e32 v113, v115
	global_store_dwordx4 v[142:143], v[120:123], off
	global_store_dwordx4 v[142:143], v[112:115], off offset:256
	s_mov_b64 s[98:99], 0x4000
	v_lshl_add_u64 v[144:145], v[142:143], 0, s[98:99]
	v_cvt_pk_bf16_f32 v107, v106, v107
	v_cvt_pk_bf16_f32 v106, v104, v105
	v_cvt_pk_bf16_f32 v104, v108, v109
	v_cvt_pk_bf16_f32 v105, v110, v111
	v_cvt_pk_bf16_f32 v99, v98, v99
	v_cvt_pk_bf16_f32 v98, v96, v97
	v_cvt_pk_bf16_f32 v96, v100, v101
	v_cvt_pk_bf16_f32 v97, v102, v103
	v_permlane32_swap_b32_e32 v104, v106
	v_permlane32_swap_b32_e32 v105, v107
	v_permlane32_swap_b32_e32 v96, v98
	v_permlane32_swap_b32_e32 v97, v99
	v_permlane16_swap_b32_e32 v104, v106
	v_permlane16_swap_b32_e32 v105, v107
	v_permlane16_swap_b32_e32 v96, v98
	v_permlane16_swap_b32_e32 v97, v99
	global_store_dwordx4 v[144:145], v[104:107], off
	global_store_dwordx4 v[144:145], v[96:99], off offset:256
	s_mov_b64 s[98:99], 0x8000
	v_lshl_add_u64 v[144:145], v[142:143], 0, s[98:99]
	v_cvt_pk_bf16_f32 v91, v90, v91
	v_cvt_pk_bf16_f32 v90, v88, v89
	v_cvt_pk_bf16_f32 v88, v92, v93
	v_cvt_pk_bf16_f32 v89, v94, v95
	v_cvt_pk_bf16_f32 v83, v82, v83
	v_cvt_pk_bf16_f32 v82, v80, v81
	v_cvt_pk_bf16_f32 v80, v84, v85
	v_cvt_pk_bf16_f32 v81, v86, v87
	v_permlane32_swap_b32_e32 v88, v90
	v_permlane32_swap_b32_e32 v89, v91
	v_permlane32_swap_b32_e32 v80, v82
	v_permlane32_swap_b32_e32 v81, v83
	v_permlane16_swap_b32_e32 v88, v90
	v_permlane16_swap_b32_e32 v89, v91
	v_permlane16_swap_b32_e32 v80, v82
	v_permlane16_swap_b32_e32 v81, v83
	global_store_dwordx4 v[144:145], v[88:91], off
	global_store_dwordx4 v[144:145], v[80:83], off offset:256
	s_mov_b64 s[98:99], 0xc000
	v_lshl_add_u64 v[144:145], v[142:143], 0, s[98:99]
	v_cvt_pk_bf16_f32 v75, v74, v75
	v_cvt_pk_bf16_f32 v74, v72, v73
	v_cvt_pk_bf16_f32 v72, v76, v77
	v_cvt_pk_bf16_f32 v73, v78, v79
	v_cvt_pk_bf16_f32 v67, v66, v67
	v_cvt_pk_bf16_f32 v66, v64, v65
	v_cvt_pk_bf16_f32 v64, v68, v69
	v_cvt_pk_bf16_f32 v65, v70, v71
	v_permlane32_swap_b32_e32 v72, v74
	v_permlane32_swap_b32_e32 v73, v75
	v_permlane32_swap_b32_e32 v64, v66
	v_permlane32_swap_b32_e32 v65, v67
	v_permlane16_swap_b32_e32 v72, v74
	v_permlane16_swap_b32_e32 v73, v75
	v_permlane16_swap_b32_e32 v64, v66
	v_permlane16_swap_b32_e32 v65, v67
	global_store_dwordx4 v[144:145], v[72:75], off
	global_store_dwordx4 v[144:145], v[64:67], off offset:256
	s_mov_b64 s[98:99], 0x20000
	v_lshl_add_u64 v[144:145], v[142:143], 0, s[98:99]
	v_cvt_pk_bf16_f32 v59, v58, v59
	v_cvt_pk_bf16_f32 v58, v56, v57
	v_cvt_pk_bf16_f32 v56, v60, v61
	v_cvt_pk_bf16_f32 v57, v62, v63
	v_cvt_pk_bf16_f32 v51, v50, v51
	v_cvt_pk_bf16_f32 v50, v48, v49
	v_cvt_pk_bf16_f32 v48, v52, v53
	v_cvt_pk_bf16_f32 v49, v54, v55
	v_permlane32_swap_b32_e32 v56, v58
	v_permlane32_swap_b32_e32 v57, v59
	v_permlane32_swap_b32_e32 v48, v50
	v_permlane32_swap_b32_e32 v49, v51
	v_permlane16_swap_b32_e32 v56, v58
	v_permlane16_swap_b32_e32 v57, v59
	v_permlane16_swap_b32_e32 v48, v50
	v_permlane16_swap_b32_e32 v49, v51
	global_store_dwordx4 v[144:145], v[56:59], off
	global_store_dwordx4 v[144:145], v[48:51], off offset:256
	s_mov_b64 s[98:99], 0x24000
	v_lshl_add_u64 v[144:145], v[142:143], 0, s[98:99]
	v_cvt_pk_bf16_f32 v43, v42, v43
	v_cvt_pk_bf16_f32 v42, v40, v41
	v_cvt_pk_bf16_f32 v40, v44, v45
	v_cvt_pk_bf16_f32 v41, v46, v47
	v_cvt_pk_bf16_f32 v35, v34, v35
	v_cvt_pk_bf16_f32 v34, v32, v33
	v_cvt_pk_bf16_f32 v32, v36, v37
	v_cvt_pk_bf16_f32 v33, v38, v39
	v_permlane32_swap_b32_e32 v40, v42
	v_permlane32_swap_b32_e32 v41, v43
	v_permlane32_swap_b32_e32 v32, v34
	v_permlane32_swap_b32_e32 v33, v35
	v_permlane16_swap_b32_e32 v40, v42
	v_permlane16_swap_b32_e32 v41, v43
	v_permlane16_swap_b32_e32 v32, v34
	v_permlane16_swap_b32_e32 v33, v35
	global_store_dwordx4 v[144:145], v[40:43], off
	global_store_dwordx4 v[144:145], v[32:35], off offset:256
	s_mov_b64 s[98:99], 0x28000
	v_lshl_add_u64 v[144:145], v[142:143], 0, s[98:99]
	v_cvt_pk_bf16_f32 v27, v26, v27
	v_cvt_pk_bf16_f32 v26, v24, v25
	v_cvt_pk_bf16_f32 v24, v28, v29
	v_cvt_pk_bf16_f32 v25, v30, v31
	v_cvt_pk_bf16_f32 v19, v18, v19
	v_cvt_pk_bf16_f32 v18, v16, v17
	v_cvt_pk_bf16_f32 v16, v20, v21
	v_cvt_pk_bf16_f32 v17, v22, v23
	v_permlane32_swap_b32_e32 v24, v26
	v_permlane32_swap_b32_e32 v25, v27
	v_permlane32_swap_b32_e32 v16, v18
	v_permlane32_swap_b32_e32 v17, v19
	v_permlane16_swap_b32_e32 v24, v26
	v_permlane16_swap_b32_e32 v25, v27
	v_permlane16_swap_b32_e32 v16, v18
	v_permlane16_swap_b32_e32 v17, v19
	global_store_dwordx4 v[144:145], v[24:27], off
	global_store_dwordx4 v[144:145], v[16:19], off offset:256
	s_mov_b64 s[98:99], 0x2c000
	v_lshl_add_u64 v[144:145], v[142:143], 0, s[98:99]
	v_cvt_pk_bf16_f32 v11, v10, v11
	v_cvt_pk_bf16_f32 v10, v8, v9
	v_cvt_pk_bf16_f32 v8, v12, v13
	v_cvt_pk_bf16_f32 v9, v14, v15
	v_cvt_pk_bf16_f32 v3, v2, v3
	v_cvt_pk_bf16_f32 v2, v0, v1
	v_cvt_pk_bf16_f32 v0, v4, v5
	v_cvt_pk_bf16_f32 v1, v6, v7
	v_permlane32_swap_b32_e32 v8, v10
	v_permlane32_swap_b32_e32 v9, v11
	v_permlane32_swap_b32_e32 v0, v2
	v_permlane32_swap_b32_e32 v1, v3
	v_permlane16_swap_b32_e32 v8, v10
	v_permlane16_swap_b32_e32 v9, v11
	v_permlane16_swap_b32_e32 v0, v2
	v_permlane16_swap_b32_e32 v1, v3
	global_store_dwordx4 v[144:145], v[8:11], off
	global_store_dwordx4 v[144:145], v[0:3], off offset:256
	s_branch .Ls5a_done
; __device__ __forceinline__ unsigned cvt_pk_bf16(float lo, float hi) { const f32x2c v = {lo, hi}; const bf16x2c b = __builtin_convertvector(v, bf16x2c); return __builtin_bit_cast(unsigned, b); }
;     __device__ __forceinline__ void operator()(const f32x4 (&acc)[2][2][4][2], const Unit& u, int wr, int wc, int fr, int fq) const {
;     ...
;             for (int m = 0; m < 4; ++m) { const size_t row = (size_t)(row0 + ai * HALF + m * 16);
; #pragma unroll
;                 for (int bj = 0; bj < 2; ++bj)
; #pragma unroll
;                     for (int n = 0; n < 2; ++n) { const int col = col0 + bj * HALF + 16 * n; const f32x4 v = acc[ai][bj][m][n];
;                         if (col < 512) { uint2 w; w.x = cvt_pk_bf16(v[0], v[1]); w.y = cvt_pk_bf16(v[2], v[3]); *(uint2*)(YI + row * 512 + col) = w; }
;                         else if (col < 640) *(f32x4*)(F + row * 128 + (col - 512)) = v; } }
.Ls5a_f:
	s_cmpk_eq_u32 s21, 0x200
	s_cbranch_scc0 .Ls5a_done
	v_lshlrev_b64 v[142:143], 9, v[140:141]
	v_lshl_add_u64 v[142:143], s[12:13], 0, v[142:143]
	v_lshlrev_b32_e32 v138, 2, v148
	v_lshl_add_u64 v[142:143], v[142:143], 0, v[138:139]
	global_store_dwordx4 v[142:143], v[124:127], off
	global_store_dwordx4 v[142:143], v[120:123], off offset:64
	s_mov_b64 s[98:99], 0x2000
	v_lshl_add_u64 v[144:145], v[142:143], 0, s[98:99]
	global_store_dwordx4 v[144:145], v[108:111], off
	global_store_dwordx4 v[144:145], v[104:107], off offset:64
	s_mov_b64 s[98:99], 0x4000
	v_lshl_add_u64 v[144:145], v[142:143], 0, s[98:99]
	global_store_dwordx4 v[144:145], v[92:95], off
	global_store_dwordx4 v[144:145], v[88:91], off offset:64
	s_mov_b64 s[98:99], 0x6000
	v_lshl_add_u64 v[144:145], v[142:143], 0, s[98:99]
	global_store_dwordx4 v[144:145], v[76:79], off
	global_store_dwordx4 v[144:145], v[72:75], off offset:64
	s_mov_b64 s[98:99], 0x10000
	v_lshl_add_u64 v[144:145], v[142:143], 0, s[98:99]
	global_store_dwordx4 v[144:145], v[60:63], off
	global_store_dwordx4 v[144:145], v[56:59], off offset:64
	s_mov_b64 s[98:99], 0x12000
	v_lshl_add_u64 v[144:145], v[142:143], 0, s[98:99]
	global_store_dwordx4 v[144:145], v[44:47], off
	global_store_dwordx4 v[144:145], v[40:43], off offset:64
	s_mov_b64 s[98:99], 0x14000
	v_lshl_add_u64 v[144:145], v[142:143], 0, s[98:99]
	global_store_dwordx4 v[144:145], v[28:31], off
	global_store_dwordx4 v[144:145], v[24:27], off offset:64
	s_mov_b64 s[98:99], 0x16000
	v_lshl_add_u64 v[144:145], v[142:143], 0, s[98:99]
	global_store_dwordx4 v[144:145], v[12:15], off
	global_store_dwordx4 v[144:145], v[8:11], off offset:64
.Ls5a_done:
	s_and_b64 vcc, exec, s[2:3]
	s_mov_b64 s[2:3], -1
	s_cbranch_vccnz .LBB0_250
